# Early barrier: the SP1 MFMA blocks of P7 (fast path) and P8 rendezvous 4 MFMAs before their end, so the partner's MFMA block starts while the last MFMAs drain
# baseline (speedup 1.0000x reference)
;     __device__ __forceinline__ void finish(v4i_t& t0, v4i_t& t1, int j, int tid) const {
;         asm volatile("" : "+v"(t0), "+v"(t1));
;         const float* s0; unsigned char* d; addr(j, tid, s0, d);
;         const f32x4 r0 = __builtin_bit_cast(f32x4, t0) * 64.f, r1 = __builtin_bit_cast(f32x4, t1) * 64.f;
;         int w0 = 0, w1 = 0; w0 = __builtin_amdgcn_cvt_pk_fp8_f32(r0[0], r1[0], w0, false); w0 = __builtin_amdgcn_cvt_pk_fp8_f32(r0[1], r1[1], w0, true);
;         w1 = __builtin_amdgcn_cvt_pk_fp8_f32(r0[2], r1[2], w1, false); w1 = __builtin_amdgcn_cvt_pk_fp8_f32(r0[3], r1[3], w1, true);
;         typedef int v2is __attribute__((ext_vector_type(2))); __builtin_nontemporal_store((v2is){w0, w1}, (v2is*)d);
.Lp7vg_wd_a1:
	s_waitcnt lgkmcnt(0)
	s_barrier
	s_cmp_lt_i32 s98, 0
	s_cbranch_scc1 .Lp7vg_mmslow_a
	s_cmpk_gt_i32 s48, 0x7f
	s_cbranch_scc1 .Lp7vg_mmslow_a
	s_setprio 1
	s_waitcnt lgkmcnt(0)
	v_mfma_scale_f32_16x16x128_f8f6f4 v[202:205], v[26:33], v[58:65], v[202:205], v226, v226 op_sel_hi:[0,0,0]
	s_add_i32 s4, s98, s52
	s_add_i32 s4, s4, 1
	v_pk_mul_f32 v[70:71], v[70:71], s[14:15] op_sel_hi:[1,0]
	v_pk_mul_f32 v[72:73], v[72:73], s[14:15] op_sel_hi:[1,0]
	v_mfma_scale_f32_16x16x128_f8f6f4 v[198:201], v[18:25], v[58:65], v[198:201], v226, v226 op_sel_hi:[0,0,0]
	v_pk_mul_f32 v[74:75], v[74:75], s[14:15] op_sel_hi:[1,0]
	v_pk_mul_f32 v[76:77], v[76:77], s[14:15] op_sel_hi:[1,0]
	s_ashr_i32 s2, s4, 10
	s_ashr_i32 s3, s2, 31
	v_mfma_scale_f32_16x16x128_f8f6f4 v[186:189], v[26:33], v[50:57], v[186:189], v226, v226 op_sel_hi:[0,0,0]
	v_cvt_pk_fp8_f32 v70, v70, v74
	s_lshl_b32 s4, s4, 12
	s_lshl_b64 s[2:3], s[2:3], 22
	v_cvt_pk_fp8_f32 v70, v71, v75 op_sel:[0,0,1]
	v_mfma_scale_f32_16x16x128_f8f6f4 v[182:185], v[18:25], v[50:57], v[182:185], v226, v226 op_sel_hi:[0,0,0]
	s_and_b32 s4, s4, 0x3ff000
	v_readlane_b32 s5, v251, 50
	v_cvt_pk_fp8_f32 v71, v72, v76
	s_add_u32 s2, s5, s2
	v_mfma_scale_f32_16x16x128_f8f6f4 v[170:173], v[26:33], v[42:49], v[170:173], v226, v226 op_sel_hi:[0,0,0]
	v_readlane_b32 s5, v251, 51
	s_addc_u32 s3, s5, s3
	v_cvt_pk_fp8_f32 v71, v73, v77 op_sel:[0,0,1]
	s_add_u32 s2, s2, s4
	s_addc_u32 s3, s3, 0
	v_mfma_scale_f32_16x16x128_f8f6f4 v[166:169], v[18:25], v[42:49], v[166:169], v226, v226 op_sel_hi:[0,0,0]
	v_lshl_add_u64 v[68:69], s[2:3], 0, v[210:211]
	global_store_dwordx2 v[68:69], v[70:71], off nt
	s_add_i32 s4, s48, s53
	s_ashr_i32 s2, s4, 10
	v_mfma_scale_f32_16x16x128_f8f6f4 v[154:157], v[26:33], v[34:41], v[154:157], v226, v226 op_sel_hi:[0,0,0]
	s_ashr_i32 s3, s2, 31
	s_lshl_b64 s[2:3], s[2:3], 24
	s_lshl_b32 s4, s4, 14
	s_and_b32 s4, s4, 0xffc000
	v_mfma_scale_f32_16x16x128_f8f6f4 v[150:153], v[18:25], v[34:41], v[150:153], v226, v226 op_sel_hi:[0,0,0]
	s_setprio 0
	s_setprio 1
	s_add_u32 s2, s76, s2
	s_addc_u32 s3, s77, s3
	s_add_u32 s2, s2, s4
	s_addc_u32 s3, s3, 0
	v_mfma_scale_f32_16x16x128_f8f6f4 v[194:197], v[10:17], v[58:65], v[194:197], v226, v226 op_sel_hi:[0,0,0]
	v_lshlrev_b32_e32 v66, 2, v208
	v_lshl_add_u64 v[68:69], s[2:3], 0, v[66:67]
	v_lshl_add_u64 v[68:69], v[68:69], 0, s[16:17]
	global_load_dwordx4 v[70:73], v66, s[2:3] nt
	v_mfma_scale_f32_16x16x128_f8f6f4 v[190:193], v[2:9], v[58:65], v[190:193], v226, v226 op_sel_hi:[0,0,0]
	global_load_dwordx4 v[74:77], v[68:69], off nt
	s_mov_b32 s100, 3
	s_mov_b32 s98, s48
	s_add_i32 s48, s48, 1
	v_mfma_scale_f32_16x16x128_f8f6f4 v[178:181], v[10:17], v[50:57], v[178:181], v226, v226 op_sel_hi:[0,0,0]
	s_add_u32 s2, s42, 0xfffc0080
	s_addc_u32 s3, s43, -1
	s_cmp_eq_u32 s64, 12
	s_cselect_b32 s5, s23, s3
	s_cselect_b32 s4, s25, s2
	s_cselect_b32 s45, s35, s63
	s_cselect_b32 s44, s61, s62
	v_mfma_scale_f32_16x16x128_f8f6f4 v[174:177], v[2:9], v[50:57], v[174:177], v226, v226 op_sel_hi:[0,0,0]
	s_barrier
	v_mfma_scale_f32_16x16x128_f8f6f4 v[162:165], v[10:17], v[42:49], v[162:165], v226, v226 op_sel_hi:[0,0,0]
	v_mfma_scale_f32_16x16x128_f8f6f4 v[158:161], v[2:9], v[42:49], v[158:161], v226, v226 op_sel_hi:[0,0,0]
	v_mfma_scale_f32_16x16x128_f8f6f4 v[146:149], v[10:17], v[34:41], v[146:149], v226, v226 op_sel_hi:[0,0,0]
	v_mfma_scale_f32_16x16x128_f8f6f4 v[142:145], v[2:9], v[34:41], v[142:145], v226, v226 op_sel_hi:[0,0,0]
	s_setprio 0
	s_branch .Lp7eb_after_a

.Lp7eb_after_a:
	s_add_u32 s2, s44, 0x1000
	s_addc_u32 s3, s45, 0
	s_mov_b32 m0, s19
	v_lshl_add_u64 v[68:69], s[44:45], 0, v[214:215]
	global_load_lds_dwordx4 v[68:69], off
	v_lshl_add_u64 v[68:69], s[44:45], 0, v[218:219]
	s_mov_b32 m0, s33
	s_nop 0
	global_load_lds_dwordx4 v[68:69], off
	v_lshl_add_u64 v[68:69], s[2:3], 0, v[214:215]
	s_mov_b32 m0, s37
	v_lshl_add_u64 v[224:225], s[4:5], 0, v[216:217]
	global_load_lds_dwordx4 v[68:69], off
	v_lshl_add_u64 v[68:69], s[2:3], 0, v[218:219]
	s_mov_b32 m0, s39
	v_cndmask_b32_e64 v66, 0, 1, s[40:41]
	global_load_lds_dwordx4 v[68:69], off
	s_andn2_b64 vcc, exec, s[40:41]
	s_cbranch_vccnz .Lhalfskip_p7a
	ds_read_b128 v[58:61], v236 offset:16384
	ds_read_b128 v[62:65], v236 offset:17408
	ds_read_b128 v[50:53], v236 offset:18432
	ds_read_b128 v[54:57], v236 offset:19456
	ds_read_b128 v[42:45], v236 offset:20480
	ds_read_b128 v[46:49], v236 offset:21504
	ds_read_b128 v[34:37], v236 offset:22528
	ds_read_b128 v[38:41], v236 offset:23552

;     __device__ __forceinline__ void finish(v4i_t& t0, v4i_t& t1, int j, int tid) const {
;         asm volatile("" : "+v"(t0), "+v"(t1));
;         const float* s0; unsigned char* d; addr(j, tid, s0, d);
;         const f32x4 r0 = __builtin_bit_cast(f32x4, t0) * 64.f, r1 = __builtin_bit_cast(f32x4, t1) * 64.f;
;         int w0 = 0, w1 = 0; w0 = __builtin_amdgcn_cvt_pk_fp8_f32(r0[0], r1[0], w0, false); w0 = __builtin_amdgcn_cvt_pk_fp8_f32(r0[1], r1[1], w0, true);
;         w1 = __builtin_amdgcn_cvt_pk_fp8_f32(r0[2], r1[2], w1, false); w1 = __builtin_amdgcn_cvt_pk_fp8_f32(r0[3], r1[3], w1, true);
;         typedef int v2is __attribute__((ext_vector_type(2))); __builtin_nontemporal_store((v2is){w0, w1}, (v2is*)d);
.Lp7vg_wd_b1:
	s_waitcnt lgkmcnt(0)
	s_barrier
	s_cmp_lt_i32 s99, 0
	s_cbranch_scc1 .Lp7vg_mmslow_b
	s_cmpk_gt_i32 s48, 0x7f
	s_cbranch_scc1 .Lp7vg_mmslow_b
	s_setprio 1
	s_waitcnt lgkmcnt(0)
	v_mfma_scale_f32_16x16x128_f8f6f4 v[202:205], v[26:33], v[58:65], v[202:205], v226, v226 op_sel_hi:[0,0,0]
	s_add_i32 s65, s99, s52
	s_add_i32 s65, s65, 1
	v_pk_mul_f32 v[242:243], v[242:243], s[14:15] op_sel_hi:[1,0]
	v_pk_mul_f32 v[244:245], v[244:245], s[14:15] op_sel_hi:[1,0]
	v_mfma_scale_f32_16x16x128_f8f6f4 v[198:201], v[18:25], v[58:65], v[198:201], v226, v226 op_sel_hi:[0,0,0]
	v_pk_mul_f32 v[246:247], v[246:247], s[14:15] op_sel_hi:[1,0]
	v_pk_mul_f32 v[248:249], v[248:249], s[14:15] op_sel_hi:[1,0]
	s_ashr_i32 s46, s65, 10
	s_ashr_i32 s47, s46, 31
	v_mfma_scale_f32_16x16x128_f8f6f4 v[186:189], v[26:33], v[50:57], v[186:189], v226, v226 op_sel_hi:[0,0,0]
	v_cvt_pk_fp8_f32 v242, v242, v246
	s_lshl_b32 s65, s65, 12
	s_lshl_b64 s[46:47], s[46:47], 22
	v_cvt_pk_fp8_f32 v242, v243, v247 op_sel:[0,0,1]
	v_mfma_scale_f32_16x16x128_f8f6f4 v[182:185], v[18:25], v[50:57], v[182:185], v226, v226 op_sel_hi:[0,0,0]
	s_and_b32 s65, s65, 0x3ff000
	v_readlane_b32 s4, v251, 50
	v_cvt_pk_fp8_f32 v243, v244, v248
	s_add_u32 s46, s4, s46
	v_mfma_scale_f32_16x16x128_f8f6f4 v[170:173], v[26:33], v[42:49], v[170:173], v226, v226 op_sel_hi:[0,0,0]
	v_readlane_b32 s4, v251, 51
	s_addc_u32 s47, s4, s47
	v_cvt_pk_fp8_f32 v243, v245, v249 op_sel:[0,0,1]
	s_add_u32 s46, s46, s65
	s_addc_u32 s47, s47, 0
	v_mfma_scale_f32_16x16x128_f8f6f4 v[166:169], v[18:25], v[42:49], v[166:169], v226, v226 op_sel_hi:[0,0,0]
	v_lshl_add_u64 v[240:241], s[46:47], 0, v[210:211]
	global_store_dwordx2 v[240:241], v[242:243], off nt
	s_add_i32 s65, s48, s53
	s_ashr_i32 s46, s65, 10
	v_mfma_scale_f32_16x16x128_f8f6f4 v[154:157], v[26:33], v[34:41], v[154:157], v226, v226 op_sel_hi:[0,0,0]
	s_ashr_i32 s47, s46, 31
	s_lshl_b64 s[46:47], s[46:47], 24
	s_lshl_b32 s65, s65, 14
	s_and_b32 s65, s65, 0xffc000
	v_mfma_scale_f32_16x16x128_f8f6f4 v[150:153], v[18:25], v[34:41], v[150:153], v226, v226 op_sel_hi:[0,0,0]
	s_setprio 0
	s_setprio 1
	s_add_u32 s46, s76, s46
	s_addc_u32 s47, s77, s47
	s_add_u32 s46, s46, s65
	s_addc_u32 s47, s47, 0
	v_mfma_scale_f32_16x16x128_f8f6f4 v[194:197], v[10:17], v[58:65], v[194:197], v226, v226 op_sel_hi:[0,0,0]
	v_lshlrev_b32_e32 v66, 2, v208
	v_lshl_add_u64 v[240:241], s[46:47], 0, v[66:67]
	v_lshl_add_u64 v[240:241], v[240:241], 0, s[16:17]
	global_load_dwordx4 v[242:245], v66, s[46:47] nt
	v_mfma_scale_f32_16x16x128_f8f6f4 v[190:193], v[2:9], v[58:65], v[190:193], v226, v226 op_sel_hi:[0,0,0]
	global_load_dwordx4 v[246:249], v[240:241], off nt
	s_mov_b32 s100, 3
	s_mov_b32 s99, s48
	s_add_i32 s48, s48, 1
	v_mfma_scale_f32_16x16x128_f8f6f4 v[178:181], v[10:17], v[50:57], v[178:181], v226, v226 op_sel_hi:[0,0,0]
	s_add_u32 s46, s44, 0x84000
	s_addc_u32 s47, s45, 0
	v_mfma_scale_f32_16x16x128_f8f6f4 v[174:177], v[2:9], v[50:57], v[174:177], v226, v226 op_sel_hi:[0,0,0]
	s_barrier
	v_mfma_scale_f32_16x16x128_f8f6f4 v[162:165], v[10:17], v[42:49], v[162:165], v226, v226 op_sel_hi:[0,0,0]
	v_mfma_scale_f32_16x16x128_f8f6f4 v[158:161], v[2:9], v[42:49], v[158:161], v226, v226 op_sel_hi:[0,0,0]
	v_mfma_scale_f32_16x16x128_f8f6f4 v[146:149], v[10:17], v[34:41], v[146:149], v226, v226 op_sel_hi:[0,0,0]
	v_mfma_scale_f32_16x16x128_f8f6f4 v[142:145], v[2:9], v[34:41], v[142:145], v226, v226 op_sel_hi:[0,0,0]
	s_setprio 0
	s_branch .Lp7eb_after_b

.Lp7eb_after_b:
	v_lshl_add_u64 v[240:241], s[46:47], 0, v[214:215]
	s_add_i32 m0, s15, 0x18000
	s_nop 0
	global_load_lds_dwordx4 v[240:241], off
	s_add_i32 m0, s15, 0x1a000
	v_lshl_add_u64 v[240:241], s[46:47], 0, v[218:219]
	global_load_lds_dwordx4 v[240:241], off
	s_add_u32 s44, s44, 0x85000
	s_addc_u32 s45, s45, 0
	v_lshl_add_u64 v[240:241], s[44:45], 0, v[214:215]
	s_add_i32 m0, s15, 0x1c000
	v_lshl_add_u64 v[68:69], v[68:69], 0, s[10:11]
	global_load_lds_dwordx4 v[240:241], off
	v_lshl_add_u64 v[240:241], s[44:45], 0, v[218:219]
	s_add_i32 m0, s15, 0x1e000
	s_nop 0
	global_load_lds_dwordx4 v[240:241], off
	s_and_b64 vcc, exec, s[2:3]
	s_cbranch_vccnz .Lhalfskip_p7b
	ds_read_b128 v[58:61], v236 offset:49152
	ds_read_b128 v[62:65], v236 offset:50176
	ds_read_b128 v[50:53], v236 offset:51200
	ds_read_b128 v[54:57], v236 offset:52224
	ds_read_b128 v[42:45], v236 offset:53248
	ds_read_b128 v[46:49], v236 offset:54272
	ds_read_b128 v[34:37], v236 offset:55296
	ds_read_b128 v[38:41], v236 offset:56320

.LBB0_901:
	ds_read_b64_tr_b16 v[26:27], v207 offset:0
	ds_read_b64_tr_b16 v[28:29], v207 offset:1024
	ds_read_b64_tr_b16 v[30:31], v207 offset:8192
	ds_read_b64_tr_b16 v[32:33], v207 offset:9216
	ds_read_b64_tr_b16 v[18:19], v217 offset:0
	ds_read_b64_tr_b16 v[20:21], v217 offset:1024
	ds_read_b64_tr_b16 v[22:23], v217 offset:8192
	ds_read_b64_tr_b16 v[24:25], v217 offset:9216
	ds_read_b64_tr_b16 v[10:11], v214 offset:0
	ds_read_b64_tr_b16 v[12:13], v214 offset:1024
	ds_read_b64_tr_b16 v[14:15], v214 offset:8192
	ds_read_b64_tr_b16 v[16:17], v214 offset:9216
	ds_read_b64_tr_b16 v[2:3], v218 offset:0
	ds_read_b64_tr_b16 v[4:5], v218 offset:1024
	ds_read_b64_tr_b16 v[6:7], v218 offset:8192
	ds_read_b64_tr_b16 v[8:9], v218 offset:9216
	s_add_u32 s2, s50, 0xfffc0080
	s_addc_u32 s3, s51, -1
	s_cmp_eq_u32 s72, 12
	s_cselect_b32 s55, s29, s3
	s_cselect_b32 s54, s31, s2
	s_cselect_b32 s53, s35, s71
	s_cselect_b32 s52, s43, s70
	ds_read_b128 v[34:37], v223
	ds_read_b128 v[38:41], v223 offset:1024
	ds_read_b128 v[42:45], v223 offset:2048
	ds_read_b128 v[46:49], v223 offset:3072
	ds_read_b128 v[50:53], v223 offset:4096
	ds_read_b128 v[54:57], v223 offset:5120
	ds_read_b128 v[58:61], v223 offset:6144
	ds_read_b128 v[62:65], v223 offset:7168
	s_waitcnt vmcnt(6)
	s_waitcnt lgkmcnt(0)
	s_barrier
	s_setprio 1
	s_waitcnt lgkmcnt(0)
	v_mfma_scale_f32_16x16x128_f8f6f4 v[194:197], v[26:33], v[34:41], v[194:197], v1, v1 op_sel_hi:[0,0,0]
	v_mfma_scale_f32_16x16x128_f8f6f4 v[190:193], v[18:25], v[34:41], v[190:193], v1, v1 op_sel_hi:[0,0,0]
	v_mfma_scale_f32_16x16x128_f8f6f4 v[186:189], v[26:33], v[42:49], v[186:189], v1, v1 op_sel_hi:[0,0,0]
	v_mfma_scale_f32_16x16x128_f8f6f4 v[182:185], v[18:25], v[42:49], v[182:185], v1, v1 op_sel_hi:[0,0,0]
	v_lshl_add_u64 v[68:69], s[50:51], 0, v[208:209]
	s_add_i32 m0, s17, 0xc000
	s_nop 0
	global_load_lds_dwordx4 v[68:69], off
	v_mfma_scale_f32_16x16x128_f8f6f4 v[162:165], v[26:33], v[50:57], v[162:165], v1, v1 op_sel_hi:[0,0,0]
	v_mfma_scale_f32_16x16x128_f8f6f4 v[158:161], v[18:25], v[50:57], v[158:161], v1, v1 op_sel_hi:[0,0,0]
	v_mfma_scale_f32_16x16x128_f8f6f4 v[146:149], v[26:33], v[58:65], v[146:149], v1, v1 op_sel_hi:[0,0,0]
	v_mfma_scale_f32_16x16x128_f8f6f4 v[142:145], v[18:25], v[58:65], v[142:145], v1, v1 op_sel_hi:[0,0,0]
	s_setprio 0
	s_setprio 1
	v_mfma_scale_f32_16x16x128_f8f6f4 v[178:181], v[10:17], v[34:41], v[178:181], v1, v1 op_sel_hi:[0,0,0]
	v_mfma_scale_f32_16x16x128_f8f6f4 v[174:177], v[2:9], v[34:41], v[174:177], v1, v1 op_sel_hi:[0,0,0]
	v_lshl_add_u64 v[68:69], s[50:51], 0, v[210:211]
	s_add_i32 m0, s17, 0xe000
	s_nop 0
	global_load_lds_dwordx4 v[68:69], off
	v_mfma_scale_f32_16x16x128_f8f6f4 v[170:173], v[10:17], v[42:49], v[170:173], v1, v1 op_sel_hi:[0,0,0]
	v_mfma_scale_f32_16x16x128_f8f6f4 v[166:169], v[2:9], v[42:49], v[166:169], v1, v1 op_sel_hi:[0,0,0]
	s_barrier
	v_mfma_scale_f32_16x16x128_f8f6f4 v[154:157], v[10:17], v[50:57], v[154:157], v1, v1 op_sel_hi:[0,0,0]
	v_mfma_scale_f32_16x16x128_f8f6f4 v[150:153], v[2:9], v[50:57], v[150:153], v1, v1 op_sel_hi:[0,0,0]
	v_mfma_scale_f32_16x16x128_f8f6f4 v[138:141], v[10:17], v[58:65], v[138:141], v1, v1 op_sel_hi:[0,0,0]
	v_mfma_scale_f32_16x16x128_f8f6f4 v[134:137], v[2:9], v[58:65], v[134:137], v1, v1 op_sel_hi:[0,0,0]
	s_setprio 0
	s_mov_b32 m0, s19
	v_lshl_add_u64 v[68:69], s[52:53], 0, v[200:201]
	global_load_lds_dwordx4 v[68:69], off
	v_lshl_add_u64 v[212:213], s[52:53], 0, v[204:205]
	s_mov_b32 m0, s33
	v_lshl_add_u64 v[68:69], v[68:69], 0, s[4:5]
	global_load_lds_dwordx4 v[212:213], off
	s_mov_b32 m0, s45
	s_nop 0
	global_load_lds_dwordx4 v[68:69], off
	v_lshl_add_u64 v[68:69], v[212:213], 0, s[4:5]
	s_mov_b32 m0, s47
	v_lshl_add_u64 v[212:213], s[54:55], 0, v[202:203]
	global_load_lds_dwordx4 v[68:69], off
	s_andn2_b64 vcc, exec, s[48:49]
	s_cbranch_vccnz .Lhalfskip_p8a
	ds_read_b128 v[58:61], v223 offset:16384
	ds_read_b128 v[62:65], v223 offset:17408
	ds_read_b128 v[50:53], v223 offset:18432
	ds_read_b128 v[54:57], v223 offset:19456
	ds_read_b128 v[42:45], v223 offset:20480
	ds_read_b128 v[46:49], v223 offset:21504
	ds_read_b128 v[34:37], v223 offset:22528
	ds_read_b128 v[38:41], v223 offset:23552

.LBB0_903:
	s_add_u32 s56, s52, 0x40000
	s_addc_u32 s57, s53, 0
	s_barrier
	ds_read_b64_tr_b16 v[26:27], v215 offset:0
	ds_read_b64_tr_b16 v[28:29], v215 offset:1024
	ds_read_b64_tr_b16 v[30:31], v215 offset:8192
	ds_read_b64_tr_b16 v[32:33], v215 offset:9216
	ds_read_b64_tr_b16 v[18:19], v219 offset:0
	ds_read_b64_tr_b16 v[20:21], v219 offset:1024
	ds_read_b64_tr_b16 v[22:23], v219 offset:8192
	ds_read_b64_tr_b16 v[24:25], v219 offset:9216
	ds_read_b64_tr_b16 v[10:11], v216 offset:0
	ds_read_b64_tr_b16 v[12:13], v216 offset:1024
	ds_read_b64_tr_b16 v[14:15], v216 offset:8192
	ds_read_b64_tr_b16 v[16:17], v216 offset:9216
	ds_read_b64_tr_b16 v[2:3], v220 offset:0
	ds_read_b64_tr_b16 v[4:5], v220 offset:1024
	ds_read_b64_tr_b16 v[6:7], v220 offset:8192
	ds_read_b64_tr_b16 v[8:9], v220 offset:9216
	s_add_u32 s54, s54, 0x40000
	s_addc_u32 s55, s55, 0
	ds_read_b128 v[34:37], v223 offset:32768
	ds_read_b128 v[38:41], v223 offset:33792
	ds_read_b128 v[42:45], v223 offset:34816
	ds_read_b128 v[46:49], v223 offset:35840
	ds_read_b128 v[50:53], v223 offset:36864
	ds_read_b128 v[54:57], v223 offset:37888
	ds_read_b128 v[58:61], v223 offset:38912
	ds_read_b128 v[62:65], v223 offset:39936
	s_waitcnt vmcnt(6)
	s_waitcnt lgkmcnt(0)
	s_barrier
	s_setprio 1
	s_waitcnt lgkmcnt(0)
	v_mfma_scale_f32_16x16x128_f8f6f4 v[194:197], v[26:33], v[34:41], v[194:197], v1, v1 op_sel_hi:[0,0,0]
	v_mfma_scale_f32_16x16x128_f8f6f4 v[190:193], v[18:25], v[34:41], v[190:193], v1, v1 op_sel_hi:[0,0,0]
	v_mfma_scale_f32_16x16x128_f8f6f4 v[186:189], v[26:33], v[42:49], v[186:189], v1, v1 op_sel_hi:[0,0,0]
	v_mfma_scale_f32_16x16x128_f8f6f4 v[182:185], v[18:25], v[42:49], v[182:185], v1, v1 op_sel_hi:[0,0,0]
	s_mov_b32 m0, s59
	v_lshl_add_u64 v[226:227], s[54:55], 0, v[198:199]
	global_load_lds_dwordx4 v[226:227], off
	v_mfma_scale_f32_16x16x128_f8f6f4 v[162:165], v[26:33], v[50:57], v[162:165], v1, v1 op_sel_hi:[0,0,0]
	v_mfma_scale_f32_16x16x128_f8f6f4 v[158:161], v[18:25], v[50:57], v[158:161], v1, v1 op_sel_hi:[0,0,0]
	v_mfma_scale_f32_16x16x128_f8f6f4 v[146:149], v[26:33], v[58:65], v[146:149], v1, v1 op_sel_hi:[0,0,0]
	v_mfma_scale_f32_16x16x128_f8f6f4 v[142:145], v[18:25], v[58:65], v[142:145], v1, v1 op_sel_hi:[0,0,0]
	s_setprio 0
	s_setprio 1
	v_mfma_scale_f32_16x16x128_f8f6f4 v[178:181], v[10:17], v[34:41], v[178:181], v1, v1 op_sel_hi:[0,0,0]
	v_mfma_scale_f32_16x16x128_f8f6f4 v[174:177], v[2:9], v[34:41], v[174:177], v1, v1 op_sel_hi:[0,0,0]
	v_lshl_add_u64 v[226:227], s[54:55], 0, v[202:203]
	s_mov_b32 m0, s60
	s_nop 0
	global_load_lds_dwordx4 v[226:227], off
	v_mfma_scale_f32_16x16x128_f8f6f4 v[170:173], v[10:17], v[42:49], v[170:173], v1, v1 op_sel_hi:[0,0,0]
	v_mfma_scale_f32_16x16x128_f8f6f4 v[166:169], v[2:9], v[42:49], v[166:169], v1, v1 op_sel_hi:[0,0,0]
	s_barrier
	v_mfma_scale_f32_16x16x128_f8f6f4 v[154:157], v[10:17], v[50:57], v[154:157], v1, v1 op_sel_hi:[0,0,0]
	v_mfma_scale_f32_16x16x128_f8f6f4 v[150:153], v[2:9], v[50:57], v[150:153], v1, v1 op_sel_hi:[0,0,0]
	v_mfma_scale_f32_16x16x128_f8f6f4 v[138:141], v[10:17], v[58:65], v[138:141], v1, v1 op_sel_hi:[0,0,0]
	v_mfma_scale_f32_16x16x128_f8f6f4 v[134:137], v[2:9], v[58:65], v[134:137], v1, v1 op_sel_hi:[0,0,0]
	s_setprio 0
	v_lshl_add_u64 v[226:227], s[56:57], 0, v[200:201]
	s_add_i32 m0, s17, 0x18000
	s_nop 0
	global_load_lds_dwordx4 v[226:227], off
	s_add_i32 m0, s17, 0x1a000
	v_lshl_add_u64 v[226:227], s[56:57], 0, v[204:205]
	global_load_lds_dwordx4 v[226:227], off
	s_add_u32 s52, s52, 0x40100
	s_addc_u32 s53, s53, 0
	v_lshl_add_u64 v[226:227], s[52:53], 0, v[200:201]
	s_add_i32 m0, s17, 0x1c000
	v_lshl_add_u64 v[68:69], v[68:69], 0, s[12:13]
	global_load_lds_dwordx4 v[226:227], off
	v_lshl_add_u64 v[226:227], s[52:53], 0, v[204:205]
	s_add_i32 m0, s17, 0x1e000
	s_nop 0
	global_load_lds_dwordx4 v[226:227], off
	s_and_b64 vcc, exec, s[2:3]
	s_cbranch_vccnz .Lhalfskip_p8b
	ds_read_b128 v[58:61], v223 offset:49152
	ds_read_b128 v[62:65], v223 offset:50176
	ds_read_b128 v[50:53], v223 offset:51200
	ds_read_b128 v[54:57], v223 offset:52224
	ds_read_b128 v[42:45], v223 offset:53248
	ds_read_b128 v[46:49], v223 offset:54272
	ds_read_b128 v[34:37], v223 offset:55296
	ds_read_b128 v[38:41], v223 offset:56320
